# prologue modulation GEMV: 4-deep software-pipelined weight-row loads (16 in flight per lane instead of 4), same accumulation order
# baseline (speedup 1.0000x reference)
.LBB0_84:
	s_mul_hi_i32 s0, s24, 0x2aaaaaab
	s_lshr_b32 s1, s0, 31
	s_ashr_i32 s0, s0, 4
	s_add_i32 s16, s0, s1
	s_mul_i32 s0, s16, 0x60
	s_sub_i32 s0, s24, s0
	s_ashr_i32 s17, s16, 31
	s_lshl_b32 s6, s0, 6
	s_lshl_b64 s[0:1], s[16:17], 10
	v_lshl_add_u64 v[14:15], s[0:1], 0, v[6:7]
	v_mad_u64_u32 v[16:17], s[0:1], v14, s25, v[12:13]
	v_mad_i32_i24 v17, v15, s25, v17
	s_ashr_i32 s7, s6, 31
	v_lshl_add_u64 v[14:15], s[6:7], 2, v[16:17]
	v_lshl_add_u64 v[14:15], v[14:15], 0, v[8:9]
	s_mov_b64 s[18:19], 0
	v_mov_b32_e32 v24, v3
	v_mov_b32_e32 v16, 0
	v_mov_b32_e32 v17, v9
	v_mov_b32_e32 v18, 0
	v_mov_b32_e32 v19, v9
	v_mov_b32_e32 v20, 0
	v_mov_b32_e32 v21, v9
	v_mov_b32_e32 v22, 0
	v_mov_b32_e32 v23, v9
	v_mov_b32_e32 v25, 0
	v_lshl_add_u64 v[26:27], v[14:15], 0, s[18:19]
	v_add_co_u32_e64 v28, s[4:5], s25, v26
	global_load_dword v62, v[26:27], off
	s_nop 0
	v_addc_co_u32_e64 v29, s[4:5], 0, v27, s[4:5]
	v_add_co_u32_e64 v30, s[4:5], s26, v26
	s_add_u32 s18, s18, 0x18000
	s_nop 0
	v_addc_co_u32_e64 v31, s[4:5], 0, v27, s[4:5]
	v_add_co_u32_e64 v26, s[4:5], s27, v26
	s_addc_u32 s19, s19, 0
	s_nop 0
	v_addc_co_u32_e64 v27, s[4:5], 0, v27, s[4:5]
	global_load_dword v64, v[28:29], off
	global_load_dword v66, v[30:31], off
	global_load_dword v68, v[26:27], off
	v_lshl_add_u64 v[26:27], v[14:15], 0, s[18:19]
	v_add_co_u32_e64 v28, s[4:5], s25, v26
	global_load_dword v78, v[26:27], off
	s_nop 0
	v_addc_co_u32_e64 v29, s[4:5], 0, v27, s[4:5]
	v_add_co_u32_e64 v30, s[4:5], s26, v26
	s_add_u32 s18, s18, 0x18000
	s_nop 0
	v_addc_co_u32_e64 v31, s[4:5], 0, v27, s[4:5]
	v_add_co_u32_e64 v26, s[4:5], s27, v26
	s_addc_u32 s19, s19, 0
	s_nop 0
	v_addc_co_u32_e64 v27, s[4:5], 0, v27, s[4:5]
	global_load_dword v80, v[28:29], off
	global_load_dword v82, v[30:31], off
	global_load_dword v84, v[26:27], off
	v_lshl_add_u64 v[26:27], v[14:15], 0, s[18:19]
	v_add_co_u32_e64 v28, s[4:5], s25, v26
	global_load_dword v86, v[26:27], off
	s_nop 0
	v_addc_co_u32_e64 v29, s[4:5], 0, v27, s[4:5]
	v_add_co_u32_e64 v30, s[4:5], s26, v26
	s_add_u32 s18, s18, 0x18000
	s_nop 0
	v_addc_co_u32_e64 v31, s[4:5], 0, v27, s[4:5]
	v_add_co_u32_e64 v26, s[4:5], s27, v26
	s_addc_u32 s19, s19, 0
	s_nop 0
	v_addc_co_u32_e64 v27, s[4:5], 0, v27, s[4:5]
	global_load_dword v88, v[28:29], off
	global_load_dword v90, v[30:31], off
	global_load_dword v92, v[26:27], off
	s_mov_b32 s52, 7
.Lgemv_loop:
	v_lshl_add_u64 v[26:27], v[14:15], 0, s[18:19]
	v_add_co_u32_e64 v28, s[4:5], s25, v26
	global_load_dword v94, v[26:27], off
	s_nop 0
	v_addc_co_u32_e64 v29, s[4:5], 0, v27, s[4:5]
	v_add_co_u32_e64 v30, s[4:5], s26, v26
	s_add_u32 s18, s18, 0x18000
	s_nop 0
	v_addc_co_u32_e64 v31, s[4:5], 0, v27, s[4:5]
	v_add_co_u32_e64 v26, s[4:5], s27, v26
	s_addc_u32 s19, s19, 0
	s_nop 0
	v_addc_co_u32_e64 v27, s[4:5], 0, v27, s[4:5]
	global_load_dword v96, v[28:29], off
	global_load_dword v98, v[30:31], off
	global_load_dword v100, v[26:27], off
	ds_read_b128 v[26:29], v24 offset:4096
	ds_read_b128 v[30:33], v24 offset:8192
	ds_read_b128 v[34:37], v24 offset:12288
	ds_read_b128 v[38:41], v24 offset:16384
	ds_read_b128 v[42:45], v24 offset:20480
	ds_read_b128 v[46:49], v24 offset:24576
	ds_read_b128 v[50:53], v24 offset:28672
	ds_read_b128 v[54:57], v24
	ds_read_b128 v[58:61], v24 offset:32768
	s_waitcnt lgkmcnt(8)
	v_mov_b32_e32 v71, v26
	s_waitcnt lgkmcnt(7)
	v_mov_b32_e32 v72, v30
	s_waitcnt lgkmcnt(6)
	v_mov_b32_e32 v73, v34
	s_waitcnt lgkmcnt(1)
	v_mov_b32_e32 v70, v54
	v_mov_b32_e32 v74, v38
	v_mov_b32_e32 v75, v42
	v_mov_b32_e32 v76, v46
	v_mov_b32_e32 v77, v50
	v_mov_b32_e32 v26, v55
	v_mov_b32_e32 v34, v31
	v_mov_b32_e32 v42, v39
	v_mov_b32_e32 v50, v47
	v_mov_b32_e32 v30, v56
	v_mov_b32_e32 v31, v28
	v_mov_b32_e32 v38, v32
	v_mov_b32_e32 v39, v36
	v_mov_b32_e32 v46, v40
	v_mov_b32_e32 v47, v44
	v_mov_b32_e32 v54, v48
	v_mov_b32_e32 v55, v52
	v_mov_b32_e32 v28, v57
	v_mov_b32_e32 v36, v33
	v_mov_b32_e32 v44, v41
	v_mov_b32_e32 v52, v49
	v_add_u32_e32 v24, 16, v24
	s_waitcnt vmcnt(15)
	v_pk_fma_f32 v[16:17], v[62:63], v[70:71], v[16:17] op_sel_hi:[0,1,1]
	v_pk_fma_f32 v[18:19], v[62:63], v[72:73], v[18:19] op_sel_hi:[0,1,1]
	v_pk_fma_f32 v[20:21], v[62:63], v[74:75], v[20:21] op_sel_hi:[0,1,1]
	v_pk_fma_f32 v[22:23], v[62:63], v[76:77], v[22:23] op_sel_hi:[0,1,1]
	s_waitcnt lgkmcnt(0)
	v_fmac_f32_e32 v25, v62, v58
	s_waitcnt vmcnt(14)
	v_pk_fma_f32 v[16:17], v[64:65], v[26:27], v[16:17] op_sel_hi:[0,1,1]
	v_pk_fma_f32 v[18:19], v[64:65], v[34:35], v[18:19] op_sel_hi:[0,1,1]
	v_pk_fma_f32 v[20:21], v[64:65], v[42:43], v[20:21] op_sel_hi:[0,1,1]
	v_pk_fma_f32 v[22:23], v[64:65], v[50:51], v[22:23] op_sel_hi:[0,1,1]
	v_fmac_f32_e32 v25, v64, v59
	s_waitcnt vmcnt(13)
	v_pk_fma_f32 v[16:17], v[66:67], v[30:31], v[16:17] op_sel_hi:[0,1,1]
	v_pk_fma_f32 v[18:19], v[66:67], v[38:39], v[18:19] op_sel_hi:[0,1,1]
	v_pk_fma_f32 v[20:21], v[66:67], v[46:47], v[20:21] op_sel_hi:[0,1,1]
	v_pk_fma_f32 v[22:23], v[66:67], v[54:55], v[22:23] op_sel_hi:[0,1,1]
	v_fmac_f32_e32 v25, v66, v60
	s_waitcnt vmcnt(12)
	v_pk_fma_f32 v[16:17], v[68:69], v[28:29], v[16:17] op_sel_hi:[0,1,1]
	v_pk_fma_f32 v[18:19], v[68:69], v[36:37], v[18:19] op_sel_hi:[0,1,1]
	v_pk_fma_f32 v[20:21], v[68:69], v[44:45], v[20:21] op_sel_hi:[0,1,1]
	v_pk_fma_f32 v[22:23], v[68:69], v[52:53], v[22:23] op_sel_hi:[0,1,1]
	v_fmac_f32_e32 v25, v68, v61
	v_lshl_add_u64 v[26:27], v[14:15], 0, s[18:19]
	v_add_co_u32_e64 v28, s[4:5], s25, v26
	global_load_dword v62, v[26:27], off
	s_nop 0
	v_addc_co_u32_e64 v29, s[4:5], 0, v27, s[4:5]
	v_add_co_u32_e64 v30, s[4:5], s26, v26
	s_add_u32 s18, s18, 0x18000
	s_nop 0
	v_addc_co_u32_e64 v31, s[4:5], 0, v27, s[4:5]
	v_add_co_u32_e64 v26, s[4:5], s27, v26
	s_addc_u32 s19, s19, 0
	s_nop 0
	v_addc_co_u32_e64 v27, s[4:5], 0, v27, s[4:5]
	global_load_dword v64, v[28:29], off
	global_load_dword v66, v[30:31], off
	global_load_dword v68, v[26:27], off
	ds_read_b128 v[26:29], v24 offset:4096
	ds_read_b128 v[30:33], v24 offset:8192
	ds_read_b128 v[34:37], v24 offset:12288
	ds_read_b128 v[38:41], v24 offset:16384
	ds_read_b128 v[42:45], v24 offset:20480
	ds_read_b128 v[46:49], v24 offset:24576
	ds_read_b128 v[50:53], v24 offset:28672
	ds_read_b128 v[54:57], v24
	ds_read_b128 v[58:61], v24 offset:32768
	s_waitcnt lgkmcnt(8)
	v_mov_b32_e32 v71, v26
	s_waitcnt lgkmcnt(7)
	v_mov_b32_e32 v72, v30
	s_waitcnt lgkmcnt(6)
	v_mov_b32_e32 v73, v34
	s_waitcnt lgkmcnt(1)
	v_mov_b32_e32 v70, v54
	v_mov_b32_e32 v74, v38
	v_mov_b32_e32 v75, v42
	v_mov_b32_e32 v76, v46
	v_mov_b32_e32 v77, v50
	v_mov_b32_e32 v26, v55
	v_mov_b32_e32 v34, v31
	v_mov_b32_e32 v42, v39
	v_mov_b32_e32 v50, v47
	v_mov_b32_e32 v30, v56
	v_mov_b32_e32 v31, v28
	v_mov_b32_e32 v38, v32
	v_mov_b32_e32 v39, v36
	v_mov_b32_e32 v46, v40
	v_mov_b32_e32 v47, v44
	v_mov_b32_e32 v54, v48
	v_mov_b32_e32 v55, v52
	v_mov_b32_e32 v28, v57
	v_mov_b32_e32 v36, v33
	v_mov_b32_e32 v44, v41
	v_mov_b32_e32 v52, v49
	v_add_u32_e32 v24, 16, v24
	s_waitcnt vmcnt(15)
	v_pk_fma_f32 v[16:17], v[78:79], v[70:71], v[16:17] op_sel_hi:[0,1,1]
	v_pk_fma_f32 v[18:19], v[78:79], v[72:73], v[18:19] op_sel_hi:[0,1,1]
	v_pk_fma_f32 v[20:21], v[78:79], v[74:75], v[20:21] op_sel_hi:[0,1,1]
	v_pk_fma_f32 v[22:23], v[78:79], v[76:77], v[22:23] op_sel_hi:[0,1,1]
	s_waitcnt lgkmcnt(0)
	v_fmac_f32_e32 v25, v78, v58
	s_waitcnt vmcnt(14)
	v_pk_fma_f32 v[16:17], v[80:81], v[26:27], v[16:17] op_sel_hi:[0,1,1]
	v_pk_fma_f32 v[18:19], v[80:81], v[34:35], v[18:19] op_sel_hi:[0,1,1]
	v_pk_fma_f32 v[20:21], v[80:81], v[42:43], v[20:21] op_sel_hi:[0,1,1]
	v_pk_fma_f32 v[22:23], v[80:81], v[50:51], v[22:23] op_sel_hi:[0,1,1]
	v_fmac_f32_e32 v25, v80, v59
	s_waitcnt vmcnt(13)
	v_pk_fma_f32 v[16:17], v[82:83], v[30:31], v[16:17] op_sel_hi:[0,1,1]
	v_pk_fma_f32 v[18:19], v[82:83], v[38:39], v[18:19] op_sel_hi:[0,1,1]
	v_pk_fma_f32 v[20:21], v[82:83], v[46:47], v[20:21] op_sel_hi:[0,1,1]
	v_pk_fma_f32 v[22:23], v[82:83], v[54:55], v[22:23] op_sel_hi:[0,1,1]
	v_fmac_f32_e32 v25, v82, v60
	s_waitcnt vmcnt(12)
	v_pk_fma_f32 v[16:17], v[84:85], v[28:29], v[16:17] op_sel_hi:[0,1,1]
	v_pk_fma_f32 v[18:19], v[84:85], v[36:37], v[18:19] op_sel_hi:[0,1,1]
	v_pk_fma_f32 v[20:21], v[84:85], v[44:45], v[20:21] op_sel_hi:[0,1,1]
	v_pk_fma_f32 v[22:23], v[84:85], v[52:53], v[22:23] op_sel_hi:[0,1,1]
	v_fmac_f32_e32 v25, v84, v61
	v_lshl_add_u64 v[26:27], v[14:15], 0, s[18:19]
	v_add_co_u32_e64 v28, s[4:5], s25, v26
	global_load_dword v78, v[26:27], off
	s_nop 0
	v_addc_co_u32_e64 v29, s[4:5], 0, v27, s[4:5]
	v_add_co_u32_e64 v30, s[4:5], s26, v26
	s_add_u32 s18, s18, 0x18000
	s_nop 0
	v_addc_co_u32_e64 v31, s[4:5], 0, v27, s[4:5]
	v_add_co_u32_e64 v26, s[4:5], s27, v26
	s_addc_u32 s19, s19, 0
	s_nop 0
	v_addc_co_u32_e64 v27, s[4:5], 0, v27, s[4:5]
	global_load_dword v80, v[28:29], off
	global_load_dword v82, v[30:31], off
	global_load_dword v84, v[26:27], off
	ds_read_b128 v[26:29], v24 offset:4096
	ds_read_b128 v[30:33], v24 offset:8192
	ds_read_b128 v[34:37], v24 offset:12288
	ds_read_b128 v[38:41], v24 offset:16384
	ds_read_b128 v[42:45], v24 offset:20480
	ds_read_b128 v[46:49], v24 offset:24576
	ds_read_b128 v[50:53], v24 offset:28672
	ds_read_b128 v[54:57], v24
	ds_read_b128 v[58:61], v24 offset:32768
	s_waitcnt lgkmcnt(8)
	v_mov_b32_e32 v71, v26
	s_waitcnt lgkmcnt(7)
	v_mov_b32_e32 v72, v30
	s_waitcnt lgkmcnt(6)
	v_mov_b32_e32 v73, v34
	s_waitcnt lgkmcnt(1)
	v_mov_b32_e32 v70, v54
	v_mov_b32_e32 v74, v38
	v_mov_b32_e32 v75, v42
	v_mov_b32_e32 v76, v46
	v_mov_b32_e32 v77, v50
	v_mov_b32_e32 v26, v55
	v_mov_b32_e32 v34, v31
	v_mov_b32_e32 v42, v39
	v_mov_b32_e32 v50, v47
	v_mov_b32_e32 v30, v56
	v_mov_b32_e32 v31, v28
	v_mov_b32_e32 v38, v32
	v_mov_b32_e32 v39, v36
	v_mov_b32_e32 v46, v40
	v_mov_b32_e32 v47, v44
	v_mov_b32_e32 v54, v48
	v_mov_b32_e32 v55, v52
	v_mov_b32_e32 v28, v57
	v_mov_b32_e32 v36, v33
	v_mov_b32_e32 v44, v41
	v_mov_b32_e32 v52, v49
	v_add_u32_e32 v24, 16, v24
	s_waitcnt vmcnt(15)
	v_pk_fma_f32 v[16:17], v[86:87], v[70:71], v[16:17] op_sel_hi:[0,1,1]
	v_pk_fma_f32 v[18:19], v[86:87], v[72:73], v[18:19] op_sel_hi:[0,1,1]
	v_pk_fma_f32 v[20:21], v[86:87], v[74:75], v[20:21] op_sel_hi:[0,1,1]
	v_pk_fma_f32 v[22:23], v[86:87], v[76:77], v[22:23] op_sel_hi:[0,1,1]
	s_waitcnt lgkmcnt(0)
	v_fmac_f32_e32 v25, v86, v58
	s_waitcnt vmcnt(14)
	v_pk_fma_f32 v[16:17], v[88:89], v[26:27], v[16:17] op_sel_hi:[0,1,1]
	v_pk_fma_f32 v[18:19], v[88:89], v[34:35], v[18:19] op_sel_hi:[0,1,1]
	v_pk_fma_f32 v[20:21], v[88:89], v[42:43], v[20:21] op_sel_hi:[0,1,1]
	v_pk_fma_f32 v[22:23], v[88:89], v[50:51], v[22:23] op_sel_hi:[0,1,1]
	v_fmac_f32_e32 v25, v88, v59
	s_waitcnt vmcnt(13)
	v_pk_fma_f32 v[16:17], v[90:91], v[30:31], v[16:17] op_sel_hi:[0,1,1]
	v_pk_fma_f32 v[18:19], v[90:91], v[38:39], v[18:19] op_sel_hi:[0,1,1]
	v_pk_fma_f32 v[20:21], v[90:91], v[46:47], v[20:21] op_sel_hi:[0,1,1]
	v_pk_fma_f32 v[22:23], v[90:91], v[54:55], v[22:23] op_sel_hi:[0,1,1]
	v_fmac_f32_e32 v25, v90, v60
	s_waitcnt vmcnt(12)
	v_pk_fma_f32 v[16:17], v[92:93], v[28:29], v[16:17] op_sel_hi:[0,1,1]
	v_pk_fma_f32 v[18:19], v[92:93], v[36:37], v[18:19] op_sel_hi:[0,1,1]
	v_pk_fma_f32 v[20:21], v[92:93], v[44:45], v[20:21] op_sel_hi:[0,1,1]
	v_pk_fma_f32 v[22:23], v[92:93], v[52:53], v[22:23] op_sel_hi:[0,1,1]
	v_fmac_f32_e32 v25, v92, v61
	v_lshl_add_u64 v[26:27], v[14:15], 0, s[18:19]
	v_add_co_u32_e64 v28, s[4:5], s25, v26
	global_load_dword v86, v[26:27], off
	s_nop 0
	v_addc_co_u32_e64 v29, s[4:5], 0, v27, s[4:5]
	v_add_co_u32_e64 v30, s[4:5], s26, v26
	s_add_u32 s18, s18, 0x18000
	s_nop 0
	v_addc_co_u32_e64 v31, s[4:5], 0, v27, s[4:5]
	v_add_co_u32_e64 v26, s[4:5], s27, v26
	s_addc_u32 s19, s19, 0
	s_nop 0
	v_addc_co_u32_e64 v27, s[4:5], 0, v27, s[4:5]
	global_load_dword v88, v[28:29], off
	global_load_dword v90, v[30:31], off
	global_load_dword v92, v[26:27], off
	ds_read_b128 v[26:29], v24 offset:4096
	ds_read_b128 v[30:33], v24 offset:8192
	ds_read_b128 v[34:37], v24 offset:12288
	ds_read_b128 v[38:41], v24 offset:16384
	ds_read_b128 v[42:45], v24 offset:20480
	ds_read_b128 v[46:49], v24 offset:24576
	ds_read_b128 v[50:53], v24 offset:28672
	ds_read_b128 v[54:57], v24
	ds_read_b128 v[58:61], v24 offset:32768
	s_waitcnt lgkmcnt(8)
	v_mov_b32_e32 v71, v26
	s_waitcnt lgkmcnt(7)
	v_mov_b32_e32 v72, v30
	s_waitcnt lgkmcnt(6)
	v_mov_b32_e32 v73, v34
	s_waitcnt lgkmcnt(1)
	v_mov_b32_e32 v70, v54
	v_mov_b32_e32 v74, v38
	v_mov_b32_e32 v75, v42
	v_mov_b32_e32 v76, v46
	v_mov_b32_e32 v77, v50
	v_mov_b32_e32 v26, v55
	v_mov_b32_e32 v34, v31
	v_mov_b32_e32 v42, v39
	v_mov_b32_e32 v50, v47
	v_mov_b32_e32 v30, v56
	v_mov_b32_e32 v31, v28
	v_mov_b32_e32 v38, v32
	v_mov_b32_e32 v39, v36
	v_mov_b32_e32 v46, v40
	v_mov_b32_e32 v47, v44
	v_mov_b32_e32 v54, v48
	v_mov_b32_e32 v55, v52
	v_mov_b32_e32 v28, v57
	v_mov_b32_e32 v36, v33
	v_mov_b32_e32 v44, v41
	v_mov_b32_e32 v52, v49
	v_add_u32_e32 v24, 16, v24
	s_waitcnt vmcnt(15)
	v_pk_fma_f32 v[16:17], v[94:95], v[70:71], v[16:17] op_sel_hi:[0,1,1]
	v_pk_fma_f32 v[18:19], v[94:95], v[72:73], v[18:19] op_sel_hi:[0,1,1]
	v_pk_fma_f32 v[20:21], v[94:95], v[74:75], v[20:21] op_sel_hi:[0,1,1]
	v_pk_fma_f32 v[22:23], v[94:95], v[76:77], v[22:23] op_sel_hi:[0,1,1]
	s_waitcnt lgkmcnt(0)
	v_fmac_f32_e32 v25, v94, v58
	s_waitcnt vmcnt(14)
	v_pk_fma_f32 v[16:17], v[96:97], v[26:27], v[16:17] op_sel_hi:[0,1,1]
	v_pk_fma_f32 v[18:19], v[96:97], v[34:35], v[18:19] op_sel_hi:[0,1,1]
	v_pk_fma_f32 v[20:21], v[96:97], v[42:43], v[20:21] op_sel_hi:[0,1,1]
	v_pk_fma_f32 v[22:23], v[96:97], v[50:51], v[22:23] op_sel_hi:[0,1,1]
	v_fmac_f32_e32 v25, v96, v59
	s_waitcnt vmcnt(13)
	v_pk_fma_f32 v[16:17], v[98:99], v[30:31], v[16:17] op_sel_hi:[0,1,1]
	v_pk_fma_f32 v[18:19], v[98:99], v[38:39], v[18:19] op_sel_hi:[0,1,1]
	v_pk_fma_f32 v[20:21], v[98:99], v[46:47], v[20:21] op_sel_hi:[0,1,1]
	v_pk_fma_f32 v[22:23], v[98:99], v[54:55], v[22:23] op_sel_hi:[0,1,1]
	v_fmac_f32_e32 v25, v98, v60
	s_waitcnt vmcnt(12)
	v_pk_fma_f32 v[16:17], v[100:101], v[28:29], v[16:17] op_sel_hi:[0,1,1]
	v_pk_fma_f32 v[18:19], v[100:101], v[36:37], v[18:19] op_sel_hi:[0,1,1]
	v_pk_fma_f32 v[20:21], v[100:101], v[44:45], v[20:21] op_sel_hi:[0,1,1]
	v_pk_fma_f32 v[22:23], v[100:101], v[52:53], v[22:23] op_sel_hi:[0,1,1]
	v_fmac_f32_e32 v25, v100, v61
	s_sub_u32 s52, s52, 1
	s_cmp_lg_u32 s52, 0
	s_cbranch_scc1 .Lgemv_loop
	v_lshl_add_u64 v[26:27], v[14:15], 0, s[18:19]
	v_add_co_u32_e64 v28, s[4:5], s25, v26
	global_load_dword v94, v[26:27], off
	s_nop 0
	v_addc_co_u32_e64 v29, s[4:5], 0, v27, s[4:5]
	v_add_co_u32_e64 v30, s[4:5], s26, v26
	s_add_u32 s18, s18, 0x18000
	s_nop 0
	v_addc_co_u32_e64 v31, s[4:5], 0, v27, s[4:5]
	v_add_co_u32_e64 v26, s[4:5], s27, v26
	s_addc_u32 s19, s19, 0
	s_nop 0
	v_addc_co_u32_e64 v27, s[4:5], 0, v27, s[4:5]
	global_load_dword v96, v[28:29], off
	global_load_dword v98, v[30:31], off
	global_load_dword v100, v[26:27], off
	ds_read_b128 v[26:29], v24 offset:4096
	ds_read_b128 v[30:33], v24 offset:8192
	ds_read_b128 v[34:37], v24 offset:12288
	ds_read_b128 v[38:41], v24 offset:16384
	ds_read_b128 v[42:45], v24 offset:20480
	ds_read_b128 v[46:49], v24 offset:24576
	ds_read_b128 v[50:53], v24 offset:28672
	ds_read_b128 v[54:57], v24
	ds_read_b128 v[58:61], v24 offset:32768
	s_waitcnt lgkmcnt(8)
	v_mov_b32_e32 v71, v26
	s_waitcnt lgkmcnt(7)
	v_mov_b32_e32 v72, v30
	s_waitcnt lgkmcnt(6)
	v_mov_b32_e32 v73, v34
	s_waitcnt lgkmcnt(1)
	v_mov_b32_e32 v70, v54
	v_mov_b32_e32 v74, v38
	v_mov_b32_e32 v75, v42
	v_mov_b32_e32 v76, v46
	v_mov_b32_e32 v77, v50
	v_mov_b32_e32 v26, v55
	v_mov_b32_e32 v34, v31
	v_mov_b32_e32 v42, v39
	v_mov_b32_e32 v50, v47
	v_mov_b32_e32 v30, v56
	v_mov_b32_e32 v31, v28
	v_mov_b32_e32 v38, v32
	v_mov_b32_e32 v39, v36
	v_mov_b32_e32 v46, v40
	v_mov_b32_e32 v47, v44
	v_mov_b32_e32 v54, v48
	v_mov_b32_e32 v55, v52
	v_mov_b32_e32 v28, v57
	v_mov_b32_e32 v36, v33
	v_mov_b32_e32 v44, v41
	v_mov_b32_e32 v52, v49
	v_add_u32_e32 v24, 16, v24
	s_waitcnt vmcnt(15)
	v_pk_fma_f32 v[16:17], v[62:63], v[70:71], v[16:17] op_sel_hi:[0,1,1]
	v_pk_fma_f32 v[18:19], v[62:63], v[72:73], v[18:19] op_sel_hi:[0,1,1]
	v_pk_fma_f32 v[20:21], v[62:63], v[74:75], v[20:21] op_sel_hi:[0,1,1]
	v_pk_fma_f32 v[22:23], v[62:63], v[76:77], v[22:23] op_sel_hi:[0,1,1]
	s_waitcnt lgkmcnt(0)
	v_fmac_f32_e32 v25, v62, v58
	s_waitcnt vmcnt(14)
	v_pk_fma_f32 v[16:17], v[64:65], v[26:27], v[16:17] op_sel_hi:[0,1,1]
	v_pk_fma_f32 v[18:19], v[64:65], v[34:35], v[18:19] op_sel_hi:[0,1,1]
	v_pk_fma_f32 v[20:21], v[64:65], v[42:43], v[20:21] op_sel_hi:[0,1,1]
	v_pk_fma_f32 v[22:23], v[64:65], v[50:51], v[22:23] op_sel_hi:[0,1,1]
	v_fmac_f32_e32 v25, v64, v59
	s_waitcnt vmcnt(13)
	v_pk_fma_f32 v[16:17], v[66:67], v[30:31], v[16:17] op_sel_hi:[0,1,1]
	v_pk_fma_f32 v[18:19], v[66:67], v[38:39], v[18:19] op_sel_hi:[0,1,1]
	v_pk_fma_f32 v[20:21], v[66:67], v[46:47], v[20:21] op_sel_hi:[0,1,1]
	v_pk_fma_f32 v[22:23], v[66:67], v[54:55], v[22:23] op_sel_hi:[0,1,1]
	v_fmac_f32_e32 v25, v66, v60
	s_waitcnt vmcnt(12)
	v_pk_fma_f32 v[16:17], v[68:69], v[28:29], v[16:17] op_sel_hi:[0,1,1]
	v_pk_fma_f32 v[18:19], v[68:69], v[36:37], v[18:19] op_sel_hi:[0,1,1]
	v_pk_fma_f32 v[20:21], v[68:69], v[44:45], v[20:21] op_sel_hi:[0,1,1]
	v_pk_fma_f32 v[22:23], v[68:69], v[52:53], v[22:23] op_sel_hi:[0,1,1]
	v_fmac_f32_e32 v25, v68, v61
	ds_read_b128 v[26:29], v24 offset:4096
	ds_read_b128 v[30:33], v24 offset:8192
	ds_read_b128 v[34:37], v24 offset:12288
	ds_read_b128 v[38:41], v24 offset:16384
	ds_read_b128 v[42:45], v24 offset:20480
	ds_read_b128 v[46:49], v24 offset:24576
	ds_read_b128 v[50:53], v24 offset:28672
	ds_read_b128 v[54:57], v24
	ds_read_b128 v[58:61], v24 offset:32768
	s_waitcnt lgkmcnt(8)
	v_mov_b32_e32 v71, v26
	s_waitcnt lgkmcnt(7)
	v_mov_b32_e32 v72, v30
	s_waitcnt lgkmcnt(6)
	v_mov_b32_e32 v73, v34
	s_waitcnt lgkmcnt(1)
	v_mov_b32_e32 v70, v54
	v_mov_b32_e32 v74, v38
	v_mov_b32_e32 v75, v42
	v_mov_b32_e32 v76, v46
	v_mov_b32_e32 v77, v50
	v_mov_b32_e32 v26, v55
	v_mov_b32_e32 v34, v31
	v_mov_b32_e32 v42, v39
	v_mov_b32_e32 v50, v47
	v_mov_b32_e32 v30, v56
	v_mov_b32_e32 v31, v28
	v_mov_b32_e32 v38, v32
	v_mov_b32_e32 v39, v36
	v_mov_b32_e32 v46, v40
	v_mov_b32_e32 v47, v44
	v_mov_b32_e32 v54, v48
	v_mov_b32_e32 v55, v52
	v_mov_b32_e32 v28, v57
	v_mov_b32_e32 v36, v33
	v_mov_b32_e32 v44, v41
	v_mov_b32_e32 v52, v49
	v_add_u32_e32 v24, 16, v24
	s_waitcnt vmcnt(11)
	v_pk_fma_f32 v[16:17], v[78:79], v[70:71], v[16:17] op_sel_hi:[0,1,1]
	v_pk_fma_f32 v[18:19], v[78:79], v[72:73], v[18:19] op_sel_hi:[0,1,1]
	v_pk_fma_f32 v[20:21], v[78:79], v[74:75], v[20:21] op_sel_hi:[0,1,1]
	v_pk_fma_f32 v[22:23], v[78:79], v[76:77], v[22:23] op_sel_hi:[0,1,1]
	s_waitcnt lgkmcnt(0)
	v_fmac_f32_e32 v25, v78, v58
	s_waitcnt vmcnt(10)
	v_pk_fma_f32 v[16:17], v[80:81], v[26:27], v[16:17] op_sel_hi:[0,1,1]
	v_pk_fma_f32 v[18:19], v[80:81], v[34:35], v[18:19] op_sel_hi:[0,1,1]
	v_pk_fma_f32 v[20:21], v[80:81], v[42:43], v[20:21] op_sel_hi:[0,1,1]
	v_pk_fma_f32 v[22:23], v[80:81], v[50:51], v[22:23] op_sel_hi:[0,1,1]
	v_fmac_f32_e32 v25, v80, v59
	s_waitcnt vmcnt(9)
	v_pk_fma_f32 v[16:17], v[82:83], v[30:31], v[16:17] op_sel_hi:[0,1,1]
	v_pk_fma_f32 v[18:19], v[82:83], v[38:39], v[18:19] op_sel_hi:[0,1,1]
	v_pk_fma_f32 v[20:21], v[82:83], v[46:47], v[20:21] op_sel_hi:[0,1,1]
	v_pk_fma_f32 v[22:23], v[82:83], v[54:55], v[22:23] op_sel_hi:[0,1,1]
	v_fmac_f32_e32 v25, v82, v60
	s_waitcnt vmcnt(8)
	v_pk_fma_f32 v[16:17], v[84:85], v[28:29], v[16:17] op_sel_hi:[0,1,1]
	v_pk_fma_f32 v[18:19], v[84:85], v[36:37], v[18:19] op_sel_hi:[0,1,1]
	v_pk_fma_f32 v[20:21], v[84:85], v[44:45], v[20:21] op_sel_hi:[0,1,1]
	v_pk_fma_f32 v[22:23], v[84:85], v[52:53], v[22:23] op_sel_hi:[0,1,1]
	v_fmac_f32_e32 v25, v84, v61
	ds_read_b128 v[26:29], v24 offset:4096
	ds_read_b128 v[30:33], v24 offset:8192
	ds_read_b128 v[34:37], v24 offset:12288
	ds_read_b128 v[38:41], v24 offset:16384
	ds_read_b128 v[42:45], v24 offset:20480
	ds_read_b128 v[46:49], v24 offset:24576
	ds_read_b128 v[50:53], v24 offset:28672
	ds_read_b128 v[54:57], v24
	ds_read_b128 v[58:61], v24 offset:32768
	s_waitcnt lgkmcnt(8)
	v_mov_b32_e32 v71, v26
	s_waitcnt lgkmcnt(7)
	v_mov_b32_e32 v72, v30
	s_waitcnt lgkmcnt(6)
	v_mov_b32_e32 v73, v34
	s_waitcnt lgkmcnt(1)
	v_mov_b32_e32 v70, v54
	v_mov_b32_e32 v74, v38
	v_mov_b32_e32 v75, v42
	v_mov_b32_e32 v76, v46
	v_mov_b32_e32 v77, v50
	v_mov_b32_e32 v26, v55
	v_mov_b32_e32 v34, v31
	v_mov_b32_e32 v42, v39
	v_mov_b32_e32 v50, v47
	v_mov_b32_e32 v30, v56
	v_mov_b32_e32 v31, v28
	v_mov_b32_e32 v38, v32
	v_mov_b32_e32 v39, v36
	v_mov_b32_e32 v46, v40
	v_mov_b32_e32 v47, v44
	v_mov_b32_e32 v54, v48
	v_mov_b32_e32 v55, v52
	v_mov_b32_e32 v28, v57
	v_mov_b32_e32 v36, v33
	v_mov_b32_e32 v44, v41
	v_mov_b32_e32 v52, v49
	v_add_u32_e32 v24, 16, v24
	s_waitcnt vmcnt(7)
	v_pk_fma_f32 v[16:17], v[86:87], v[70:71], v[16:17] op_sel_hi:[0,1,1]
	v_pk_fma_f32 v[18:19], v[86:87], v[72:73], v[18:19] op_sel_hi:[0,1,1]
	v_pk_fma_f32 v[20:21], v[86:87], v[74:75], v[20:21] op_sel_hi:[0,1,1]
	v_pk_fma_f32 v[22:23], v[86:87], v[76:77], v[22:23] op_sel_hi:[0,1,1]
	s_waitcnt lgkmcnt(0)
	v_fmac_f32_e32 v25, v86, v58
	s_waitcnt vmcnt(6)
	v_pk_fma_f32 v[16:17], v[88:89], v[26:27], v[16:17] op_sel_hi:[0,1,1]
	v_pk_fma_f32 v[18:19], v[88:89], v[34:35], v[18:19] op_sel_hi:[0,1,1]
	v_pk_fma_f32 v[20:21], v[88:89], v[42:43], v[20:21] op_sel_hi:[0,1,1]
	v_pk_fma_f32 v[22:23], v[88:89], v[50:51], v[22:23] op_sel_hi:[0,1,1]
	v_fmac_f32_e32 v25, v88, v59
	s_waitcnt vmcnt(5)
	v_pk_fma_f32 v[16:17], v[90:91], v[30:31], v[16:17] op_sel_hi:[0,1,1]
	v_pk_fma_f32 v[18:19], v[90:91], v[38:39], v[18:19] op_sel_hi:[0,1,1]
	v_pk_fma_f32 v[20:21], v[90:91], v[46:47], v[20:21] op_sel_hi:[0,1,1]
	v_pk_fma_f32 v[22:23], v[90:91], v[54:55], v[22:23] op_sel_hi:[0,1,1]
	v_fmac_f32_e32 v25, v90, v60
	s_waitcnt vmcnt(4)
	v_pk_fma_f32 v[16:17], v[92:93], v[28:29], v[16:17] op_sel_hi:[0,1,1]
	v_pk_fma_f32 v[18:19], v[92:93], v[36:37], v[18:19] op_sel_hi:[0,1,1]
	v_pk_fma_f32 v[20:21], v[92:93], v[44:45], v[20:21] op_sel_hi:[0,1,1]
	v_pk_fma_f32 v[22:23], v[92:93], v[52:53], v[22:23] op_sel_hi:[0,1,1]
	v_fmac_f32_e32 v25, v92, v61
	ds_read_b128 v[26:29], v24 offset:4096
	ds_read_b128 v[30:33], v24 offset:8192
	ds_read_b128 v[34:37], v24 offset:12288
	ds_read_b128 v[38:41], v24 offset:16384
	ds_read_b128 v[42:45], v24 offset:20480
	ds_read_b128 v[46:49], v24 offset:24576
	ds_read_b128 v[50:53], v24 offset:28672
	ds_read_b128 v[54:57], v24
	ds_read_b128 v[58:61], v24 offset:32768
	s_waitcnt lgkmcnt(8)
	v_mov_b32_e32 v71, v26
	s_waitcnt lgkmcnt(7)
	v_mov_b32_e32 v72, v30
	s_waitcnt lgkmcnt(6)
	v_mov_b32_e32 v73, v34
	s_waitcnt lgkmcnt(1)
	v_mov_b32_e32 v70, v54
	v_mov_b32_e32 v74, v38
	v_mov_b32_e32 v75, v42
	v_mov_b32_e32 v76, v46
	v_mov_b32_e32 v77, v50
	v_mov_b32_e32 v26, v55
	v_mov_b32_e32 v34, v31
	v_mov_b32_e32 v42, v39
	v_mov_b32_e32 v50, v47
	v_mov_b32_e32 v30, v56
	v_mov_b32_e32 v31, v28
	v_mov_b32_e32 v38, v32
	v_mov_b32_e32 v39, v36
	v_mov_b32_e32 v46, v40
	v_mov_b32_e32 v47, v44
	v_mov_b32_e32 v54, v48
	v_mov_b32_e32 v55, v52
	v_mov_b32_e32 v28, v57
	v_mov_b32_e32 v36, v33
	v_mov_b32_e32 v44, v41
	v_mov_b32_e32 v52, v49
	v_add_u32_e32 v24, 16, v24
	s_waitcnt vmcnt(3)
	v_pk_fma_f32 v[16:17], v[94:95], v[70:71], v[16:17] op_sel_hi:[0,1,1]
	v_pk_fma_f32 v[18:19], v[94:95], v[72:73], v[18:19] op_sel_hi:[0,1,1]
	v_pk_fma_f32 v[20:21], v[94:95], v[74:75], v[20:21] op_sel_hi:[0,1,1]
	v_pk_fma_f32 v[22:23], v[94:95], v[76:77], v[22:23] op_sel_hi:[0,1,1]
	s_waitcnt lgkmcnt(0)
	v_fmac_f32_e32 v25, v94, v58
	s_waitcnt vmcnt(2)
	v_pk_fma_f32 v[16:17], v[96:97], v[26:27], v[16:17] op_sel_hi:[0,1,1]
	v_pk_fma_f32 v[18:19], v[96:97], v[34:35], v[18:19] op_sel_hi:[0,1,1]
	v_pk_fma_f32 v[20:21], v[96:97], v[42:43], v[20:21] op_sel_hi:[0,1,1]
	v_pk_fma_f32 v[22:23], v[96:97], v[50:51], v[22:23] op_sel_hi:[0,1,1]
	v_fmac_f32_e32 v25, v96, v59
	s_waitcnt vmcnt(1)
	v_pk_fma_f32 v[16:17], v[98:99], v[30:31], v[16:17] op_sel_hi:[0,1,1]
	v_pk_fma_f32 v[18:19], v[98:99], v[38:39], v[18:19] op_sel_hi:[0,1,1]
	v_pk_fma_f32 v[20:21], v[98:99], v[46:47], v[20:21] op_sel_hi:[0,1,1]
	v_pk_fma_f32 v[22:23], v[98:99], v[54:55], v[22:23] op_sel_hi:[0,1,1]
	v_fmac_f32_e32 v25, v98, v60
	s_waitcnt vmcnt(0)
	v_pk_fma_f32 v[16:17], v[100:101], v[28:29], v[16:17] op_sel_hi:[0,1,1]
	v_pk_fma_f32 v[18:19], v[100:101], v[36:37], v[18:19] op_sel_hi:[0,1,1]
	v_pk_fma_f32 v[20:21], v[100:101], v[44:45], v[20:21] op_sel_hi:[0,1,1]
	v_pk_fma_f32 v[22:23], v[100:101], v[52:53], v[22:23] op_sel_hi:[0,1,1]
	v_fmac_f32_e32 v25, v100, v61
	v_add_u32_e32 v14, 64, v5
	ds_write2st64_b32 v14, v16, v17 offset0:144 offset1:145
	ds_write2st64_b32 v14, v18, v19 offset0:146 offset1:147
	ds_write2st64_b32 v14, v20, v21 offset0:148 offset1:149
	ds_write2st64_b32 v14, v22, v23 offset0:150 offset1:151
	ds_write_b32 v5, v25 offset:38976
	s_waitcnt lgkmcnt(0)
	s_barrier
	s_and_saveexec_b64 s[0:1], vcc
	s_cbranch_execz .LBB0_83
	s_mul_i32 s4, s16, 0x1800
	s_add_i32 s4, s4, s6
	v_or_b32_e32 v14, s4, v4
	v_ashrrev_i32_e32 v15, 31, v14
	s_mul_hi_i32 s17, s16, 9
	s_mul_i32 s16, s16, 9
	v_lshl_add_u64 v[14:15], v[14:15], 2, s[20:21]
	v_lshl_add_u64 v[16:17], s[6:7], 2, v[10:11]
	s_mov_b64 s[6:7], 0
	v_mov_b32_e32 v18, v2
